# v69 + flagged-row index/threshold read before the candidate barrier
# baseline (speedup 1.0000x reference)
.LBB0_116:
	s_or_b64 exec, exec, s[0:1]
	v_or_b32_e32 v66, s25, v181
	v_cmp_lt_u32_e32 vcc, v66, v183
	v_mov_b32_e32 v67, 0
	v_mov_b32_e32 v186, 0
	v_mov_b32_e32 v187, 0
	v_mov_b32_e32 v168, 0xff61b1e6
	s_and_saveexec_b64 s[0:1], vcc
	v_lshl_add_u32 v68, v66, 2, v249
	ds_read_b32 v67, v68
	v_lshl_add_u32 v68, v66, 2, v250
	ds_read_b32 v168, v68
	s_or_b64 exec, exec, s[0:1]
	s_waitcnt lgkmcnt(0)
	s_barrier
	v_mul_lo_u32 v67, v67, s3
	v_add_u32_e32 v67, v182, v67
	ds_read_b128 v[162:165], v67
	ds_read_b128 v[94:97], v67 offset:32
	ds_read_b128 v[90:93], v67 offset:64
	ds_read_b128 v[86:89], v67 offset:96
	s_waitcnt lgkmcnt(3)
	v_mfma_f32_32x32x16_f16 v[66:81], v[98:101], v[162:165], v[2:17]
	s_waitcnt lgkmcnt(2)
	v_mfma_f32_32x32x16_f16 v[66:81], v[102:105], v[94:97], v[66:81]
	s_waitcnt lgkmcnt(1)
	v_mfma_f32_32x32x16_f16 v[66:81], v[106:109], v[90:93], v[66:81]
	s_waitcnt lgkmcnt(0)
	v_mfma_f32_32x32x16_f16 v[66:81], v[110:113], v[86:89], v[66:81]
	s_nop 11
	v_min3_f32 v254, v66, v67, v68
	v_min3_f32 v254, v254, v69, v70
	v_min3_f32 v254, v254, v71, v72
	v_min3_f32 v254, v254, v73, v74
	v_min3_f32 v254, v254, v75, v76
	v_min3_f32 v254, v254, v77, v78
	v_min3_f32 v254, v254, v79, v80
	v_min_f32_e32 v254, v254, v81
	v_cmp_lt_f32_e32 vcc, v254, v168
	s_cbranch_vccz .Lrc_skip_tile0
	v_mov_b32_e32 v254, 0
	v_cmp_lt_f32_e64 s[0:1], v81, v168
	v_cmp_lt_f32_e64 s[14:15], v80, v168
	v_cmp_lt_f32_e64 s[16:17], v79, v168
	v_addc_co_u32_e64 v254, vcc, v254, v254, s[0:1]
	v_cmp_lt_f32_e64 s[0:1], v78, v168
	v_addc_co_u32_e64 v254, vcc, v254, v254, s[14:15]
	v_cmp_lt_f32_e64 s[14:15], v77, v168
	v_addc_co_u32_e64 v254, vcc, v254, v254, s[16:17]
	v_cmp_lt_f32_e64 s[16:17], v76, v168
	v_addc_co_u32_e64 v254, vcc, v254, v254, s[0:1]
	v_cmp_lt_f32_e64 s[0:1], v75, v168
	v_addc_co_u32_e64 v254, vcc, v254, v254, s[14:15]
	v_cmp_lt_f32_e64 s[14:15], v74, v168
	v_addc_co_u32_e64 v254, vcc, v254, v254, s[16:17]
	v_cmp_lt_f32_e64 s[16:17], v73, v168
	v_addc_co_u32_e64 v254, vcc, v254, v254, s[0:1]
	v_cmp_lt_f32_e64 s[0:1], v72, v168
	v_addc_co_u32_e64 v254, vcc, v254, v254, s[14:15]
	v_cmp_lt_f32_e64 s[14:15], v71, v168
	v_addc_co_u32_e64 v254, vcc, v254, v254, s[16:17]
	v_cmp_lt_f32_e64 s[16:17], v70, v168
	v_addc_co_u32_e64 v254, vcc, v254, v254, s[0:1]
	v_cmp_lt_f32_e64 s[0:1], v69, v168
	v_addc_co_u32_e64 v254, vcc, v254, v254, s[14:15]
	v_cmp_lt_f32_e64 s[14:15], v68, v168
	v_addc_co_u32_e64 v254, vcc, v254, v254, s[16:17]
	v_cmp_lt_f32_e64 s[16:17], v67, v168
	v_addc_co_u32_e64 v254, vcc, v254, v254, s[0:1]
	v_cmp_lt_f32_e64 s[0:1], v66, v168
	v_addc_co_u32_e64 v254, vcc, v254, v254, s[14:15]
	v_addc_co_u32_e64 v254, vcc, v254, v254, s[16:17]
	v_addc_co_u32_e64 v254, vcc, v254, v254, s[0:1]
	v_or_b32_e32 v186, v186, v254
